# conversion-in-attention, deferred: a unit's loads go out behind the attention loads and it is packed at the end of the NEXT iteration (two-iteration latency budget)
# speedup vs baseline: 1.0065x; 1.0065x over previous
; #define LAS __attribute__((address_space(3)))
; __device__ __forceinline__ void convert_experts(Frame& F, int lo, int hi) {
;     const int gw = F.vcu * 8 + F.wave, NGW = F.G * 8;
;     LAS unsigned char* scr = F.lds + F.wave * 16384;
;     unsigned char* W1t = WSP(F, WS_W1T, unsigned char); unsigned char* W2t = WSP(F, WS_W2T, unsigned char);
;     const float* weg = F.a->in[I_WEG]; const float* weu = F.a->in[I_WEU]; const float* wed = F.a->in[I_WED];
;     const float* wsg = F.a->in[I_WSG]; const float* wsu = F.a->in[I_WSU]; const float* wsd = F.a->in[I_WSD];
;     ...
;     constexpr int NPAIRS = CONV_ITEMS / 2;
;     (void)lo; (void)hi;
;     ...
;     if (gw < NPAIRS) {
;         const int ns = 2 * ((NPAIRS - gw + NGW - 1) / NGW);
;         int sq = 0, r = CONV_RIDX(0);
;         TItem tc, tn; CONV_DESC(r, tc); tn = tc;
;         int p = 0; bool first = true;
.Lcva_vcu:
	s_lshr_b32 s99, s99, 6
	s_lshl_b32 s101, s101, 3
	s_add_u32 s89, s101, s99
	s_movk_i32 s90, 12
	s_lshr_b32 s32, s89, 3
	s_and_b32 s32, s32, 3
	s_cmp_ge_u32 s32, 4
	s_cselect_b32 s99, 4, 0
	s_sub_u32 s32, s32, s99
	s_mov_b32 s95, 0
	s_waitcnt vmcnt(0)
	s_branch .LBB0_304

; #define LAS __attribute__((address_space(3)))
; __device__ __forceinline__ void lds_barrier() { asm volatile("s_waitcnt lgkmcnt(0)\n\ts_barrier" ::: "memory"); }
; __device__ __forceinline__ void phase_attn(Frame& F) {
;     ...
;     for (; jl < PER_X; jl += G8) {
;         lds_barrier();
;         LAS unsigned char* kb = F.lds + buf * ABUF;
.LBB0_304:
	s_mul_i32 s37, s79, 0x12000
	s_add_i32 s85, s37, 0
	s_cmp_eq_u32 s95, 0
	s_cbranch_scc1 .Lcva_w3
	s_cmp_eq_u32 s32, 3
	s_cbranch_scc0 .Lcva_w7
	s_waitcnt vmcnt(19)
	s_branch .Lcva_wd
.Lcva_w7:
	s_waitcnt vmcnt(7)
	s_mov_b32 s95, 0
	s_branch .Lcva_wd

; __device__ __forceinline__ void phase_attn(Frame& F) {
;     ...
;         lds_barrier();
;         LAS unsigned char* kb = F.lds + buf * ABUF;
;         const bf16x8 q0 = qn0, q1 = qn1;
;         {
;             LAS unsigned char* ob = F.lds + (buf ^ 1) * ABUF;
; #pragma unroll
;             for (int jj = 0; jj < 4; ++jj) { const int ch = tid + 512 * jj, row = ch >> 3, c16 = ch & 7;
;                 *(LAS u32x4*)(ob + row * ATT_ROWB + c16 * 16) = kr[jj]; *(LAS u32x4*)(ob + ATT_VOFF + row * ATT_ROWB + c16 * 16) = vr[jj]; }
;         }
;         const AttnUnit nu = un;
;         un = attn_decode(x8 * PER_X + (jl + 2 * G8 < jlast ? jl + 2 * G8 : jlast)); attn_issue(qkv, un, tid, kr, vr);
;         { const char* qb = (const char*)qkv + (((size_t)nu.b * SEQ + nu.r) * NPROJ + nu.h * 64) * 2; const unsigned qo = __umul24((unsigned)(128 * nu.n + ql), (unsigned)nu.d * (NPROJ * 2)) + 16u * fq;
;           qn0 = *(const bf16x8*)(qb + qo); qn1 = *(const bf16x8*)(qb + qo + 64); }
;         const unsigned qrow = __umul24((unsigned)(128 * cu.n + ql), (unsigned)cu.d);
;         const float c1 = 0.125f * LOG2E;
;         const float nc2 = -__builtin_amdgcn_exp2f(-(float)(cu.h + 1)) * (float)cu.d * LOG2E;
;         const bool first = cu.n == 0;
;         f32x4 St[9];
;         const f32x4 eb = (f32x4){ef[0], ef[1], ef[2], ef[3]} * nc2;
;         float mx = -INFINITY;
;         bf16x8 kf[9][2];
; #pragma unroll
;         for (int T = 0; T < 9; ++T) { LAS unsigned char* ka = kb + (16 * (w + T) + fr) * ATT_ROWB + fq * 16; kf[T][0] = *(LAS bf16x8*)ka; kf[T][1] = *(LAS bf16x8*)(ka + 64); }
;         __builtin_amdgcn_sched_barrier(0);
; #pragma unroll
;         for (int T = 0; T < 9; ++T) {
;             f32x4 sa = (f32x4){0.f, 0.f, 0.f, 0.f};
;             sa = __builtin_amdgcn_mfma_f32_16x16x32_bf16(kf[T][0], q0, sa, 0, 0, 0);
;             sa = __builtin_amdgcn_mfma_f32_16x16x32_bf16(kf[T][1], q1, sa, 0, 0, 0);
;             const float kT = (!first || w + T >= 8) ? nc2 * (float)(128 - 16 * T) : -INFINITY;
;             sa = sa * c1 + (eb + kT);
; #pragma unroll
;             for (int rg = 0; rg < 4; ++rg) {
;                 if (T == 0) sa[rg] = ef[rg] <= 0.f ? sa[rg] : -INFINITY;
;                 if (T == 8) sa[rg] = ef[rg] >= 0.f ? sa[rg] : -INFINITY;
;             }
;             St[T] = sa;
;             mx = fmaxf(mx, fmaxf(fmaxf(sa[0], sa[1]), fmaxf(sa[2], sa[3])));
.Lcva_wd:
	v_mov_b64_e32 v[48:49], v[4:5]
	v_mov_b64_e32 v[46:47], v[2:3]
	v_mov_b64_e32 v[44:45], v[8:9]
	v_mov_b64_e32 v[42:43], v[6:7]
	s_lshl_b32 s65, 1, s35
	s_waitcnt lgkmcnt(0)
	s_barrier
	s_add_i32 s37, s30, 1
	v_cvt_f32_u32_e32 v54, s37
	v_cvt_f32_u32_e32 v55, s65
	v_add_u32_e32 v110, s85, v82
	v_add_u32_e32 v58, v110, v90
	v_exp_f32_e64 v54, -v54
	v_add_u32_e32 v66, v110, v91
	v_add_u32_e32 v74, v110, v92
	v_add_u32_e32 v111, v110, v93
	v_mul_f32_e32 v79, v55, v54
	ds_read_b128 v[54:57], v58
	ds_read_b128 v[58:61], v58 offset:64
	ds_read_b128 v[62:65], v66
	ds_read_b128 v[66:69], v66 offset:64
	ds_read_b128 v[70:73], v74
	ds_read_b128 v[74:77], v74 offset:64
	ds_read_b128 v[112:115], v111
	ds_read_b128 v[116:119], v111 offset:64
	v_add_u32_e32 v111, v110, v94
	ds_read_b128 v[120:123], v111
	ds_read_b128 v[124:127], v111 offset:64
	v_add_u32_e32 v111, v110, v95
	ds_read_b128 v[128:131], v111
	ds_read_b128 v[132:135], v111 offset:64
	v_add_u32_e32 v111, v110, v96
	ds_read_b128 v[136:139], v111
	ds_read_b128 v[140:143], v111 offset:64
	v_add_u32_e32 v111, v110, v97
	v_add_u32_e32 v110, v110, v98
	ds_read_b128 v[144:147], v111
	ds_read_b128 v[148:151], v111 offset:64
	ds_read_b128 v[152:155], v110
	ds_read_b128 v[156:159], v110 offset:64
	s_cmp_lg_u32 s64, 0
	v_lshl_add_u32 v78, s64, 7, v86
	s_cselect_b64 s[64:65], -1, 0
	v_mul_f32_e32 v160, 0xbfb8aa3b, v79
	v_and_b32_e32 v110, 0xffffff, v78
	s_waitcnt lgkmcnt(14)
	v_mfma_f32_16x16x32_bf16 v[54:57], v[54:57], v[46:49], 0
	v_mul_f32_e32 v78, 0x43000000, v160
	s_or_b64 vcc, s[64:65], s[38:39]
	v_cndmask_b32_e32 v78, v109, v78, vcc
	v_mfma_f32_16x16x32_bf16 v[54:57], v[58:61], v[42:45], v[54:57]
	v_fma_f32 v162, v50, v160, v78
	v_fma_f32 v163, v51, v160, v78
	v_pk_fma_f32 v[78:79], v[52:53], v[160:161], v[78:79] op_sel_hi:[1,0,0]
	s_or_b64 vcc, s[64:65], s[40:41]
	s_nop 3
	v_pk_fma_f32 v[56:57], v[56:57], s[56:57], v[78:79] op_sel_hi:[1,0,1]
	v_pk_fma_f32 v[54:55], v[54:55], s[56:57], v[162:163] op_sel_hi:[1,0,1]
	v_cndmask_b32_e64 v164, v109, v56, s[10:11]
	v_cndmask_b32_e64 v162, v109, v54, s[6:7]
	v_cndmask_b32_e64 v163, v109, v55, s[8:9]
	v_cndmask_b32_e64 v165, v109, v57, s[12:13]
	v_mfma_f32_16x16x32_bf16 v[54:57], v[62:65], v[46:49], 0
	v_max_f32_e32 v58, v162, v163
	v_max_f32_e32 v59, v164, v165
	v_max3_f32 v62, v58, v59, s78
	v_mfma_f32_16x16x32_bf16 v[54:57], v[66:69], v[42:45], v[54:57]
	v_mul_f32_e32 v58, 0x42e00000, v160
	v_cndmask_b32_e32 v58, v109, v58, vcc
	v_pk_fma_f32 v[60:61], v[50:51], v[160:161], v[58:59] op_sel_hi:[1,0,0]
	v_pk_fma_f32 v[58:59], v[52:53], v[160:161], v[58:59] op_sel_hi:[1,0,0]
	s_or_b64 vcc, s[64:65], s[42:43]
	s_nop 2
	v_pk_fma_f32 v[166:167], v[56:57], s[56:57], v[58:59] op_sel_hi:[1,0,1]
	s_waitcnt lgkmcnt(13)
	v_mfma_f32_16x16x32_bf16 v[56:59], v[70:73], v[46:49], 0
	v_fma_f32 v78, v54, s56, v60
	v_fma_f32 v79, v55, s56, v61
	v_max_f32_e32 v54, v166, v167
	v_max3_f32 v63, v78, v79, v54
	s_waitcnt lgkmcnt(12)
	v_mfma_f32_16x16x32_bf16 v[54:57], v[74:77], v[42:45], v[56:59]
	s_nop 2
	v_mul_f32_e32 v58, 0x42c00000, v160
	v_cndmask_b32_e32 v58, v109, v58, vcc
	v_pk_fma_f32 v[60:61], v[50:51], v[160:161], v[58:59] op_sel_hi:[1,0,0]
	v_pk_fma_f32 v[58:59], v[52:53], v[160:161], v[58:59] op_sel_hi:[1,0,0]
	s_nop 0
	v_pk_fma_f32 v[76:77], v[54:55], s[56:57], v[60:61] op_sel_hi:[1,0,1]
	v_pk_fma_f32 v[74:75], v[56:57], s[56:57], v[58:59] op_sel_hi:[1,0,1]
	s_waitcnt lgkmcnt(11)
	v_mfma_f32_16x16x32_bf16 v[54:57], v[112:115], v[46:49], 0
	v_max_f32_e32 v58, v74, v75
	v_max3_f32 v58, v76, v77, v58
	v_max3_f32 v62, v62, v63, v58
	s_waitcnt lgkmcnt(10)
	v_mfma_f32_16x16x32_bf16 v[54:57], v[116:119], v[42:45], v[54:57]
	v_mul_f32_e32 v58, 0x42a00000, v160
	s_or_b64 vcc, s[64:65], s[44:45]
	v_cndmask_b32_e32 v58, v109, v58, vcc
	v_pk_fma_f32 v[60:61], v[50:51], v[160:161], v[58:59] op_sel_hi:[1,0,0]
	v_pk_fma_f32 v[58:59], v[52:53], v[160:161], v[58:59] op_sel_hi:[1,0,0]
	s_nop 2
	v_pk_fma_f32 v[72:73], v[54:55], s[56:57], v[60:61] op_sel_hi:[1,0,1]
	v_pk_fma_f32 v[70:71], v[56:57], s[56:57], v[58:59] op_sel_hi:[1,0,1]
	s_waitcnt lgkmcnt(9)
	v_mfma_f32_16x16x32_bf16 v[56:59], v[120:123], v[46:49], 0
	v_max_f32_e32 v54, v70, v71
	v_max3_f32 v63, v72, v73, v54
	s_or_b64 vcc, s[64:65], s[46:47]
	s_waitcnt lgkmcnt(8)
	v_mfma_f32_16x16x32_bf16 v[54:57], v[124:127], v[42:45], v[56:59]
	s_nop 2
	v_mul_f32_e32 v58, 0x42800000, v160
	v_cndmask_b32_e32 v58, v109, v58, vcc
	v_pk_fma_f32 v[60:61], v[50:51], v[160:161], v[58:59] op_sel_hi:[1,0,0]
	v_pk_fma_f32 v[58:59], v[52:53], v[160:161], v[58:59] op_sel_hi:[1,0,0]
	s_nop 0
	v_pk_fma_f32 v[68:69], v[54:55], s[56:57], v[60:61] op_sel_hi:[1,0,1]
	v_pk_fma_f32 v[66:67], v[56:57], s[56:57], v[58:59] op_sel_hi:[1,0,1]
	s_waitcnt lgkmcnt(7)
	v_mfma_f32_16x16x32_bf16 v[54:57], v[128:131], v[46:49], 0
	v_max_f32_e32 v58, v66, v67
	v_max3_f32 v58, v68, v69, v58
	v_max3_f32 v111, v62, v63, v58
	s_waitcnt lgkmcnt(6)
	v_mfma_f32_16x16x32_bf16 v[54:57], v[132:135], v[42:45], v[54:57]
	v_mul_f32_e32 v58, 0x42400000, v160
	s_or_b64 vcc, s[64:65], s[48:49]
	v_cndmask_b32_e32 v58, v109, v58, vcc
	v_pk_fma_f32 v[60:61], v[50:51], v[160:161], v[58:59] op_sel_hi:[1,0,0]
	v_pk_fma_f32 v[58:59], v[52:53], v[160:161], v[58:59] op_sel_hi:[1,0,0]
	s_nop 2
	v_pk_fma_f32 v[64:65], v[54:55], s[56:57], v[60:61] op_sel_hi:[1,0,1]
	v_pk_fma_f32 v[62:63], v[56:57], s[56:57], v[58:59] op_sel_hi:[1,0,1]
	s_waitcnt lgkmcnt(5)
	v_mfma_f32_16x16x32_bf16 v[56:59], v[136:139], v[46:49], 0
	v_max_f32_e32 v54, v62, v63
	v_max3_f32 v112, v64, v65, v54
	s_or_b64 vcc, s[64:65], s[50:51]
	s_waitcnt lgkmcnt(4)
; #define LAS __attribute__((address_space(3)))
; __device__ __forceinline__ void phase_attn(Frame& F) {
;     ...
;             LAS unsigned char* ob = F.lds + (buf ^ 1) * ABUF;
; #pragma unroll
;             for (int jj = 0; jj < 4; ++jj) { const int ch = tid + 512 * jj, row = ch >> 3, c16 = ch & 7;
;                 *(LAS u32x4*)(ob + row * ATT_ROWB + c16 * 16) = kr[jj]; *(LAS u32x4*)(ob + ATT_VOFF + row * ATT_ROWB + c16 * 16) = vr[jj]; }
;         }
;         const AttnUnit nu = un;
;         un = attn_decode(x8 * PER_X + (jl + 2 * G8 < jlast ? jl + 2 * G8 : jlast)); attn_issue(qkv, un, tid, kr, vr);
;         { const char* qb = (const char*)qkv + (((size_t)nu.b * SEQ + nu.r) * NPROJ + nu.h * 64) * 2; const unsigned qo = __umul24((unsigned)(128 * nu.n + ql), (unsigned)nu.d * (NPROJ * 2)) + 16u * fq;
;           qn0 = *(const bf16x8*)(qb + qo); qn1 = *(const bf16x8*)(qb + qo + 64); }
	v_mfma_f32_16x16x32_bf16 v[54:57], v[140:143], v[42:45], v[56:59]
	s_nop 2
	v_mul_f32_e32 v58, 0x42000000, v160
	v_cndmask_b32_e32 v58, v109, v58, vcc
	v_pk_fma_f32 v[60:61], v[50:51], v[160:161], v[58:59] op_sel_hi:[1,0,0]
	v_pk_fma_f32 v[58:59], v[52:53], v[160:161], v[58:59] op_sel_hi:[1,0,0]
	s_nop 0
	v_pk_fma_f32 v[60:61], v[54:55], s[56:57], v[60:61] op_sel_hi:[1,0,1]
	v_pk_fma_f32 v[58:59], v[56:57], s[56:57], v[58:59] op_sel_hi:[1,0,1]
	s_waitcnt lgkmcnt(3)
	v_mfma_f32_16x16x32_bf16 v[54:57], v[144:147], v[46:49], 0
	v_max_f32_e32 v113, v58, v59
	v_max3_f32 v113, v60, v61, v113
	v_max3_f32 v111, v111, v112, v113
	s_waitcnt lgkmcnt(1)
	v_mfma_f32_16x16x32_bf16 v[46:49], v[152:155], v[46:49], 0
	s_or_b64 vcc, s[64:65], s[52:53]
	v_add_u32_e32 v144, s85, v89
	v_add_u32_e32 v130, v144, v99
	v_mfma_f32_16x16x32_bf16 v[112:115], v[148:151], v[42:45], v[54:57]
	v_add_u32_e32 v140, v144, v100
	v_add_u32_e32 v145, v144, v101
	s_nop 0
	v_mul_f32_e32 v54, 0x41800000, v160
	s_waitcnt lgkmcnt(0)
	v_mfma_f32_16x16x32_bf16 v[42:45], v[156:159], v[42:45], v[46:49]
	s_add_i32 s37, s77, s70
	s_xor_b32 s79, s79, 1
	s_min_i32 s37, s37, s71
	s_mul_i32 s58, s79, 0x12000
	s_add_i32 s37, s37, s3
	v_add_u32_e32 v2, s58, v84
	s_mul_hi_i32 s58, s37, 0x2aaaaaab
	s_lshr_b32 s59, s58, 31
	s_ashr_i32 s58, s58, 4
	s_add_i32 s59, s58, s59
	s_mul_i32 s58, s59, 0x60
	s_sub_i32 s37, s37, s58
	s_ashr_i32 s58, s59, 3
	s_and_b32 s80, s59, 7
	v_add_u32_e32 v3, v2, v83
	s_cmp_gt_i32 s37, 31
	ds_write_b128 v3, v[38:41]
	ds_write_b128 v3, v[34:37] offset:36864
	v_add_u32_e32 v3, v2, v85
	s_cselect_b64 s[82:83], -1, 0
	s_cmp_gt_i32 s37, 63
	ds_write_b128 v3, v[30:33]
	ds_write_b128 v3, v[26:29] offset:36864
	v_add_u32_e32 v3, v2, v87
	v_add_u32_e32 v2, v2, v88
	s_cselect_b64 s[86:87], -1, 0
	ds_write_b128 v3, v[22:25]
	ds_write_b128 v3, v[18:21] offset:36864
	ds_write_b128 v2, v[14:17]
	ds_write_b128 v2, v[10:13] offset:36864
	v_cndmask_b32_e64 v2, 0, 1, s[86:87]
	s_cmp_lg_u64 s[82:83], 0
	v_readfirstlane_b32 s59, v2
	s_addc_u32 s81, s59, 0
	s_lshl_b32 s59, s81, 5
	s_lshl_b32 s82, s81, 1
	s_sub_i32 s37, s37, s59
	s_sub_i32 s59, 5, s82
	s_ashr_i32 s83, s37, s59
	s_lshl_b32 s59, -1, s59
	s_andn2_b32 s84, s37, s59
	s_ashr_i32 s59, s58, 31
	s_lshl_b64 s[86:87], s[58:59], 12
	s_ashr_i32 s37, s83, 31
	s_add_u32 s59, s86, s83
	s_addc_u32 s37, s87, s37
	s_mulk_i32 s37, 0xa00
	s_mul_hi_u32 s86, s59, 0xa00
	s_add_i32 s87, s86, s37
	s_mulk_i32 s59, 0xa00
	s_lshl_b32 s37, s80, 6
	s_or_b32 s86, s59, s37
	s_lshl_b64 s[86:87], s[86:87], 1
	s_add_u32 s37, s33, s86
	s_addc_u32 s59, s66, s87
	s_add_u32 s86, s37, 0x400
	s_addc_u32 s87, s59, 0
	s_lshl_b32 s59, s84, 7
	v_add_u32_e32 v2, s59, v81
	s_lshl_b32 s37, 0x1400, s82
	v_max_i32_e32 v3, 0, v2
	v_mul_u32_u24_e32 v3, s37, v3
	v_or_b32_e32 v3, v3, v80
	global_load_dwordx4 v[38:41], v3, s[86:87]
	global_load_dwordx4 v[34:37], v3, s[86:87] offset:1024
	v_max_i32_e32 v3, 0xffffffc0, v2
	v_add_u32_e32 v3, 64, v3
	v_mul_u32_u24_e32 v3, s37, v3
	v_or_b32_e32 v3, v3, v80
	global_load_dwordx4 v[30:33], v3, s[86:87]
	global_load_dwordx4 v[26:29], v3, s[86:87] offset:1024
	v_add_u32_e32 v3, s59, v1
	v_max_i32_e32 v2, 0xffffff40, v2
	v_max_i32_e32 v3, 0, v3
	v_add_u32_e32 v2, 0xc0, v2
	v_mul_u32_u24_e32 v3, s37, v3
	v_mul_u32_u24_e32 v2, s37, v2
	v_or_b32_e32 v3, v3, v80
	v_or_b32_e32 v2, v2, v80
	s_ashr_i32 s37, s36, 31
	global_load_dwordx4 v[22:25], v3, s[86:87]
	global_load_dwordx4 v[18:21], v3, s[86:87] offset:1024
	global_load_dwordx4 v[14:17], v2, s[86:87]
	global_load_dwordx4 v[10:13], v2, s[86:87] offset:1024
	s_lshl_b64 s[86:87], s[36:37], 12
	s_ashr_i32 s37, s73, 31
	s_add_u32 s59, s86, s73
	s_addc_u32 s37, s87, s37
	s_mulk_i32 s37, 0xa00
	s_mul_hi_u32 s86, s59, 0xa00
	s_add_i32 s87, s86, s37
	s_mulk_i32 s59, 0xa00
	s_lshl_b32 s37, s75, 6
	s_or_b32 s86, s59, s37
	s_lshl_b64 s[86:87], s[86:87], 1
	s_add_u32 s86, s33, s86
	s_addc_u32 s87, s66, s87
	s_lshl_b32 s37, 0x1400, s74
	v_lshl_add_u32 v2, s76, 7, v86
	s_and_b32 s37, s37, 0x555400
	v_mul_u32_u24_e32 v2, s37, v2
	v_or_b32_e32 v6, v2, v82
	global_load_dwordx4 v[2:5], v6, s[86:87]
	s_nop 0
	global_load_dwordx4 v[6:9], v6, s[86:87] offset:64
	s_sub_u32 s32, s32, 1
	s_cmp_lt_i32 s32, 0
	s_cbranch_scc0 .Lcva_none_l
	s_mov_b32 s32, 3
	s_cmp_eq_u32 s90, 0
	s_cbranch_scc1 .Lcva_none_l
	s_sub_u32 s90, s90, 1
	s_lshr_b32 s98, s89, 6
	s_and_b32 s99, s89, 63
	s_mul_hi_u32 s100, s98, 0xaaaaaaab
	s_lshr_b32 s100, s100, 1
	s_mul_i32 s101, s100, 3
	s_sub_u32 s101, s98, s101
	s_cmp_lt_u32 s100, 256
	s_cselect_b32 s98, 0, 3
	s_cselect_b32 s95, s100, 0
	s_add_u32 s98, s98, s101
	s_lshl_b32 s98, s98, 1
	v_readlane_b32 s96, v253, s98
	s_add_u32 s98, s98, 1
	v_readlane_b32 s97, v253, s98
	s_lshl_b32 s95, s95, 20
	s_nop 3
	s_add_u32 s96, s96, s95
	s_addc_u32 s97, s97, 0
	s_cmp_eq_u32 s101, 2
	s_cbranch_scc1 .Lcva_down_l
	s_lshr_b32 s95, s99, 3
	s_and_b32 s99, s99, 7
	s_lshl_b32 s98, s95, 17
	s_add_u32 s96, s96, s98
	s_addc_u32 s97, s97, 0
	s_lshl_b32 s98, s99, 7
	s_add_u32 s96, s96, s98
	s_addc_u32 s97, s97, 0
	s_lshl_b32 s100, s100, 19
	s_lshr_b32 s98, s99, 2
	s_lshl_b32 s98, s98, 18
	s_add_u32 s100, s100, s98
	s_and_b32 s98, s99, 3
	s_lshl_b32 s98, s98, 15
	s_add_u32 s100, s100, s98
	s_lshl_b32 s98, s101, 17
	s_add_u32 s100, s100, s98
	s_lshl_b32 s98, s95, 7
	s_add_u32 s100, s100, s98
	v_readlane_b32 s92, v253, 12
	v_readlane_b32 s93, v253, 13
	s_mov_b32 s94, 0xc3317218
	s_cmp_eq_u32 s101, 0
	s_cselect_b32 s94, 0xc2b8aa3b, s94
	s_nop 3
	s_add_u32 s92, s92, s100
	s_addc_u32 s93, s93, 0
	s_movk_i32 s95, 0x400
	s_movk_i32 s98, 0x400
	s_branch .Lcva_go_l

; #define LAS __attribute__((address_space(3)))
; __device__ __forceinline__ unsigned cvt_pk_bf16(float lo, float hi) { const f32x2_t v = {lo, hi}; return __builtin_bit_cast(unsigned, __builtin_convertvector(v, bf16x2_t)); }
; __device__ __forceinline__ float fast_exp2(float x) { return __builtin_amdgcn_exp2f(x); }
; __device__ __forceinline__ s16x4 tr_read(LAS unsigned char* p) { return __builtin_bit_cast(s16x4, __builtin_amdgcn_ds_read_tr16_b64_v4i16((LAS s16x4*)p)); }
; __device__ __forceinline__ void phase_attn(Frame& F) {
;     ...
;         mx = fmaxf(mx, __shfl_xor(mx, 16)); mx = fmaxf(mx, __shfl_xor(mx, 32));
;         f32x4 lv = (f32x4){0.f, 0.f, 0.f, 0.f};
;         f32x4 nmx = (f32x4){-mx, -mx, -mx, -mx}; asm volatile("" : "+v"(nmx));
; #pragma unroll
;         for (int T = 0; T < 9; ++T) { const f32x4 d = St[T] + nmx; f32x4 pv; pv.x = fast_exp2(d.x); pv.y = fast_exp2(d.y); pv.z = fast_exp2(d.z); pv.w = fast_exp2(d.w); St[T] = pv; lv = lv + pv; }
;         float l = (lv.x + lv.y) + (lv.z + lv.w);
;         l += __shfl_xor(l, 16); l += __shfl_xor(l, 32);
;         f32x4 O[4];
; #pragma unroll
;         for (int dt = 0; dt < 4; ++dt) O[dt] = (f32x4){0.f, 0.f, 0.f, 0.f};
; #pragma unroll
;         for (int T = 0; T < 9; ++T) {
;             u32x2 pw; pw.x = cvt_pk_bf16(St[T][0], St[T][1]); pw.y = cvt_pk_bf16(St[T][2], St[T][3]);
;             const s16x4 pb = __builtin_bit_cast(s16x4, pw);
;             LAS unsigned char* va = kb + ATT_VOFF + (16 * (w + T) + 4 * fq + (fr >> 2)) * ATT_ROWB + (8 * (fr & 3)) * 2;
; #pragma unroll
;             for (int dt = 0; dt < 4; ++dt) O[dt] = __builtin_amdgcn_mfma_f32_16x16x16bf16_1k(tr_read(va + 64 * (dt >> 1) + 8 * (dt & 1)), pb, O[dt], 0, 0, 0);
.Lcva_none_l:
	v_cndmask_b32_e32 v54, v109, v54, vcc
	s_or_b64 vcc, s[64:65], s[54:55]
	v_pk_fma_f32 v[56:57], v[50:51], v[160:161], v[54:55] op_sel_hi:[1,0,0]
	v_mul_f32_e32 v46, 0, v160
	v_cndmask_b32_e32 v46, v109, v46, vcc
	v_pk_fma_f32 v[48:49], v[50:51], v[160:161], v[46:47] op_sel_hi:[1,0,0]
	v_pk_fma_f32 v[46:47], v[52:53], v[160:161], v[46:47] op_sel_hi:[1,0,0]
	v_pk_fma_f32 v[54:55], v[52:53], v[160:161], v[54:55] op_sel_hi:[1,0,0]
	v_pk_fma_f32 v[44:45], v[44:45], s[56:57], v[46:47] op_sel_hi:[1,0,1]
	v_pk_fma_f32 v[42:43], v[42:43], s[56:57], v[48:49] op_sel_hi:[1,0,1]
	v_cndmask_b32_e64 v48, v109, v44, s[18:19]
	v_and_b32_e32 v44, 64, v108
	v_pk_fma_f32 v[54:55], v[114:115], s[56:57], v[54:55] op_sel_hi:[1,0,1]
	v_cndmask_b32_e64 v47, v109, v43, s[16:17]
	v_cndmask_b32_e64 v49, v109, v45, s[20:21]
	v_xor_b32_e32 v43, 16, v108
	v_add_u32_e32 v44, 64, v44
	v_pk_fma_f32 v[56:57], v[112:113], s[56:57], v[56:57] op_sel_hi:[1,0,1]
	v_max_f32_e32 v112, v54, v55
	v_cndmask_b32_e64 v46, v109, v42, s[14:15]
	v_max_f32_e32 v42, v48, v49
	v_cmp_lt_i32_e32 vcc, v43, v44
	v_max3_f32 v112, v56, v57, v112
	v_max3_f32 v42, v46, v47, v42
	v_cndmask_b32_e32 v43, v108, v43, vcc
	v_max3_f32 v42, v111, v112, v42
	v_lshlrev_b32_e32 v142, 2, v43
	ds_bpermute_b32 v43, v142, v42
	s_waitcnt lgkmcnt(0)
	v_max_f32_e32 v43, v43, v43
	v_max_f32_e32 v42, v42, v43
	v_xor_b32_e32 v43, 32, v108
	v_cmp_lt_i32_e32 vcc, v43, v44
	s_nop 1
	v_cndmask_b32_e32 v43, v108, v43, vcc
	v_lshlrev_b32_e32 v143, 2, v43
	ds_bpermute_b32 v43, v143, v42
	s_waitcnt lgkmcnt(0)
	v_max_f32_e32 v43, v43, v43
	v_max_f32_e32 v111, v42, v43
	v_xor_b32_e32 v42, 0x80000000, v111
	v_mov_b32_e32 v43, v42
	v_mov_b32_e32 v44, v42
	v_mov_b32_e32 v45, v42
	ds_read_b64_tr_b16 v[120:121], v130 offset:36864
	v_pk_add_f32 v[118:119], v[166:167], v[44:45]
	v_pk_add_f32 v[112:113], v[164:165], v[44:45]
	v_exp_f32_e32 v126, v118
	v_exp_f32_e32 v127, v119
	ds_read_b64_tr_b16 v[118:119], v130 offset:36872
	v_pk_add_f32 v[114:115], v[162:163], v[42:43]
	v_exp_f32_e32 v112, v112
	v_exp_f32_e32 v114, v114
	v_exp_f32_e32 v113, v113
	v_exp_f32_e32 v115, v115
	ds_read_b64_tr_b16 v[128:129], v130 offset:36928
	ds_read_b64_tr_b16 v[130:131], v130 offset:36936
	v_pk_add_f32 v[134:135], v[76:77], v[42:43]
	v_cvt_pk_bf16_f32 v123, v112, v113
	v_cvt_pk_bf16_f32 v122, v114, v115
	v_pk_add_f32 v[116:117], v[112:113], 0 op_sel_hi:[1,0]
	v_pk_add_f32 v[124:125], v[114:115], 0 op_sel_hi:[1,0]
	s_waitcnt lgkmcnt(3)
	v_mfma_f32_16x16x16_bf16 v[112:115], v[120:121], v[122:123], 0
	v_add_f32_e64 v120, v74, v44
	v_add_f32_e64 v121, v75, v45
	v_pk_add_f32 v[132:133], v[126:127], v[116:117]
	v_exp_f32_e32 v136, v120
	s_waitcnt lgkmcnt(2)
	v_mfma_f32_16x16x16_bf16 v[116:119], v[118:119], v[122:123], 0
	v_exp_f32_e32 v137, v121
	v_pk_add_f32 v[78:79], v[78:79], v[42:43]
	v_cvt_pk_bf16_f32 v139, v126, v127
	s_waitcnt lgkmcnt(1)
	v_mfma_f32_16x16x16_bf16 v[74:77], v[128:129], v[122:123], 0
	ds_read_b64_tr_b16 v[128:129], v140 offset:36864
	v_exp_f32_e32 v78, v78
	v_exp_f32_e32 v79, v79
	s_waitcnt lgkmcnt(1)
	v_mfma_f32_16x16x16_bf16 v[120:123], v[130:131], v[122:123], 0
	ds_read_b64_tr_b16 v[130:131], v140 offset:36872
	ds_read_b64_tr_b16 v[126:127], v140 offset:36928
	ds_read_b64_tr_b16 v[140:141], v140 offset:36936
	v_cvt_pk_bf16_f32 v138, v78, v79
	v_exp_f32_e32 v134, v134
	v_exp_f32_e32 v135, v135
	s_waitcnt lgkmcnt(3)
	v_mfma_f32_16x16x16_bf16 v[112:115], v[128:129], v[138:139], v[112:115]
	v_add_f32_e64 v128, v70, v44
	v_add_f32_e64 v129, v71, v45
	v_pk_add_f32 v[78:79], v[78:79], v[124:125]
	v_pk_add_f32 v[124:125], v[136:137], v[132:133]
	s_waitcnt lgkmcnt(2)
	v_mfma_f32_16x16x16_bf16 v[116:119], v[130:131], v[138:139], v[116:119]
	v_add_f32_e64 v130, v72, v42
	v_add_f32_e64 v131, v73, v43
	v_pk_add_f32 v[78:79], v[134:135], v[78:79]
	v_exp_f32_e32 v128, v128
	s_waitcnt lgkmcnt(1)
	v_mfma_f32_16x16x16_bf16 v[70:73], v[126:127], v[138:139], v[74:77]
	ds_read_b64_tr_b16 v[126:127], v145 offset:36864
	v_exp_f32_e32 v129, v129
	v_pk_add_f32 v[48:49], v[44:45], v[48:49]
	s_waitcnt lgkmcnt(1)
	v_mfma_f32_16x16x16_bf16 v[74:77], v[140:141], v[138:139], v[120:123]
	v_add_f32_e64 v124, v128, v124
	v_add_f32_e64 v125, v129, v125
	s_nop 0
	ds_read_b64_tr_b16 v[120:121], v145 offset:36872
	v_cvt_pk_bf16_f32 v122, v134, v135
	ds_read_b64_tr_b16 v[132:133], v145 offset:36928
	ds_read_b64_tr_b16 v[134:135], v145 offset:36936
	v_cvt_pk_bf16_f32 v123, v136, v137
	v_add_u32_e32 v136, v144, v102
	s_waitcnt lgkmcnt(3)
	v_mfma_f32_16x16x16_bf16 v[112:115], v[126:127], v[122:123], v[112:115]
	v_exp_f32_e32 v126, v130
	v_exp_f32_e32 v127, v131
	v_pk_add_f32 v[130:131], v[68:69], v[42:43]
	s_waitcnt lgkmcnt(2)
	v_mfma_f32_16x16x16_bf16 v[116:119], v[120:121], v[122:123], v[116:119]
	v_add_f32_e64 v120, v66, v44
	v_add_f32_e64 v121, v67, v45
	v_pk_add_f32 v[78:79], v[126:127], v[78:79]
	v_exp_f32_e32 v130, v130
	s_waitcnt lgkmcnt(1)
	v_mfma_f32_16x16x16_bf16 v[66:69], v[132:133], v[122:123], v[70:73]
	ds_read_b64_tr_b16 v[132:133], v136 offset:36864
	v_exp_f32_e32 v120, v120
	v_exp_f32_e32 v121, v121
	s_waitcnt lgkmcnt(1)
	v_mfma_f32_16x16x16_bf16 v[70:73], v[134:135], v[122:123], v[74:77]
	ds_read_b64_tr_b16 v[122:123], v136 offset:36872
	v_cvt_pk_bf16_f32 v134, v126, v127
	v_cvt_pk_bf16_f32 v135, v128, v129
	ds_read_b64_tr_b16 v[128:129], v136 offset:36928
	ds_read_b64_tr_b16 v[136:137], v136 offset:36936
	s_waitcnt lgkmcnt(3)
	v_mfma_f32_16x16x16_bf16 v[74:77], v[132:133], v[134:135], v[112:115]
	v_add_u32_e32 v132, v144, v103
	ds_read_b64_tr_b16 v[126:127], v132 offset:36872
	v_exp_f32_e32 v131, v131
	s_waitcnt lgkmcnt(3)
; #define LAS __attribute__((address_space(3)))
; __device__ __forceinline__ unsigned cvt_pk_bf16(float lo, float hi) { const f32x2_t v = {lo, hi}; return __builtin_bit_cast(unsigned, __builtin_convertvector(v, bf16x2_t)); }
; __device__ __forceinline__ float fast_exp2(float x) { return __builtin_amdgcn_exp2f(x); }
; __device__ __forceinline__ s16x4 tr_read(LAS unsigned char* p) { return __builtin_bit_cast(s16x4, __builtin_amdgcn_ds_read_tr16_b64_v4i16((LAS s16x4*)p)); }
; __device__ __forceinline__ void phase_attn(Frame& F) {
;     ...
;         for (int T = 0; T < 9; ++T) { const f32x4 d = St[T] + nmx; f32x4 pv; pv.x = fast_exp2(d.x); pv.y = fast_exp2(d.y); pv.z = fast_exp2(d.z); pv.w = fast_exp2(d.w); St[T] = pv; lv = lv + pv; }
;         float l = (lv.x + lv.y) + (lv.z + lv.w);
;         l += __shfl_xor(l, 16); l += __shfl_xor(l, 32);
;         f32x4 O[4];
; #pragma unroll
;         for (int dt = 0; dt < 4; ++dt) O[dt] = (f32x4){0.f, 0.f, 0.f, 0.f};
; #pragma unroll
;         for (int T = 0; T < 9; ++T) {
;             u32x2 pw; pw.x = cvt_pk_bf16(St[T][0], St[T][1]); pw.y = cvt_pk_bf16(St[T][2], St[T][3]);
;             const s16x4 pb = __builtin_bit_cast(s16x4, pw);
;             LAS unsigned char* va = kb + ATT_VOFF + (16 * (w + T) + 4 * fq + (fr >> 2)) * ATT_ROWB + (8 * (fr & 3)) * 2;
; #pragma unroll
;             for (int dt = 0; dt < 4; ++dt) O[dt] = __builtin_amdgcn_mfma_f32_16x16x16bf16_1k(tr_read(va + 64 * (dt >> 1) + 8 * (dt & 1)), pb, O[dt], 0, 0, 0);
;         }
;         const float inv = 1.f / l;
;         bf16_t* op = (bf16_t*)((char*)part + (((size_t)cu.dsel * NTOK + (size_t)cu.b * SEQ + cu.r) * 512 + cu.h * 64) * 2 + (qrow * 1024u + 16u * fq));
; #pragma unroll
;         for (int u2 = 0; u2 < 2; ++u2) { u32x4 o4; o4.x = cvt_pk_bf16(O[2 * u2][0] * inv, O[2 * u2][1] * inv); o4.y = cvt_pk_bf16(O[2 * u2][2] * inv, O[2 * u2][3] * inv);
;             o4.z = cvt_pk_bf16(O[2 * u2 + 1][0] * inv, O[2 * u2 + 1][1] * inv); o4.w = cvt_pk_bf16(O[2 * u2 + 1][2] * inv, O[2 * u2 + 1][3] * inv); *(u32x4*)(op + 32 * u2) = o4; }
	v_mfma_f32_16x16x16_bf16 v[112:115], v[122:123], v[134:135], v[116:119]
	ds_read_b64_tr_b16 v[122:123], v132 offset:36864
	v_pk_add_f32 v[124:125], v[120:121], v[124:125]
	v_pk_add_f32 v[78:79], v[130:131], v[78:79]
	v_pk_add_f32 v[116:117], v[62:63], v[44:45]
	v_pk_add_f32 v[118:119], v[64:65], v[42:43]
	s_waitcnt lgkmcnt(3)
	v_mfma_f32_16x16x16_bf16 v[62:65], v[128:129], v[134:135], v[66:69]
	v_exp_f32_e32 v116, v116
	v_exp_f32_e32 v117, v117
	v_cvt_pk_bf16_f32 v128, v130, v131
	v_cvt_pk_bf16_f32 v129, v120, v121
	ds_read_b64_tr_b16 v[120:121], v132 offset:36928
	ds_read_b64_tr_b16 v[130:131], v132 offset:36936
	v_add_u32_e32 v132, v144, v104
	s_waitcnt lgkmcnt(4)
	v_mfma_f32_16x16x16_bf16 v[66:69], v[136:137], v[134:135], v[70:73]
	v_exp_f32_e32 v118, v118
	v_exp_f32_e32 v119, v119
	s_waitcnt lgkmcnt(2)
	v_mfma_f32_16x16x16_bf16 v[70:73], v[122:123], v[128:129], v[74:77]
	v_add_f32_e64 v122, v116, v124
	v_add_f32_e64 v123, v117, v125
	ds_read_b64_tr_b16 v[124:125], v132 offset:36872
	v_pk_add_f32 v[78:79], v[118:119], v[78:79]
	v_mfma_f32_16x16x16_bf16 v[74:77], v[126:127], v[128:129], v[112:115]
	v_cvt_pk_bf16_f32 v127, v116, v117
	v_cvt_pk_bf16_f32 v126, v118, v119
	s_nop 0
	v_pk_add_f32 v[112:113], v[58:59], v[44:45]
	v_pk_add_f32 v[114:115], v[60:61], v[42:43]
	s_waitcnt lgkmcnt(2)
	v_mfma_f32_16x16x16_bf16 v[58:61], v[120:121], v[128:129], v[62:65]
	ds_read_b64_tr_b16 v[120:121], v132 offset:36864
	v_exp_f32_e32 v112, v112
	v_exp_f32_e32 v113, v113
	v_exp_f32_e32 v114, v114
	s_waitcnt lgkmcnt(2)
	v_mfma_f32_16x16x16_bf16 v[62:65], v[130:131], v[128:129], v[66:69]
	ds_read_b64_tr_b16 v[116:117], v132 offset:36928
	ds_read_b64_tr_b16 v[128:129], v132 offset:36936
	v_exp_f32_e32 v115, v115
	v_pk_add_f32 v[118:119], v[112:113], v[122:123]
	v_add_u32_e32 v122, v144, v105
	s_waitcnt lgkmcnt(2)
	v_mfma_f32_16x16x16_bf16 v[66:69], v[120:121], v[126:127], v[70:73]
	ds_read_b64_tr_b16 v[120:121], v122 offset:36872
	v_mfma_f32_16x16x16_bf16 v[70:73], v[124:125], v[126:127], v[74:77]
	s_nop 2
	v_add_f32_e64 v74, v114, v78
	v_add_f32_e64 v75, v115, v79
	v_pk_add_f32 v[76:77], v[54:55], v[44:45]
	v_pk_add_f32 v[78:79], v[56:57], v[42:43]
	s_waitcnt lgkmcnt(2)
	v_mfma_f32_16x16x16_bf16 v[54:57], v[116:117], v[126:127], v[58:61]
	ds_read_b64_tr_b16 v[116:117], v122 offset:36864
	v_cvt_pk_bf16_f32 v114, v114, v115
	v_cvt_pk_bf16_f32 v115, v112, v113
	ds_read_b64_tr_b16 v[112:113], v122 offset:36928
	ds_read_b64_tr_b16 v[122:123], v122 offset:36936
	s_waitcnt lgkmcnt(4)
	v_mfma_f32_16x16x16_bf16 v[58:61], v[128:129], v[126:127], v[62:65]
	v_exp_f32_e32 v76, v76
	v_exp_f32_e32 v77, v77
	v_exp_f32_e32 v78, v78
	s_waitcnt lgkmcnt(2)
	v_mfma_f32_16x16x16_bf16 v[62:65], v[116:117], v[114:115], v[66:69]
	v_exp_f32_e32 v79, v79
	v_pk_add_f32 v[116:117], v[76:77], v[118:119]
	v_mfma_f32_16x16x16_bf16 v[66:69], v[120:121], v[114:115], v[70:73]
	s_nop 2
	v_add_f32_e64 v70, v42, v46
	v_add_f32_e64 v71, v43, v47
	s_waitcnt lgkmcnt(1)
	v_mfma_f32_16x16x16_bf16 v[42:45], v[112:113], v[114:115], v[54:57]
	v_exp_f32_e32 v72, v48
	v_exp_f32_e32 v73, v49
	v_exp_f32_e32 v70, v70
	v_add_u32_e32 v56, v144, v106
	ds_read_b64_tr_b16 v[54:55], v56 offset:36864
	s_waitcnt lgkmcnt(1)
	v_mfma_f32_16x16x16_bf16 v[46:49], v[122:123], v[114:115], v[58:61]
	v_exp_f32_e32 v71, v71
	v_cvt_pk_bf16_f32 v112, v78, v79
	v_cvt_pk_bf16_f32 v113, v76, v77
	ds_read_b64_tr_b16 v[58:59], v56 offset:36872
	ds_read_b64_tr_b16 v[76:77], v56 offset:36928
	ds_read_b64_tr_b16 v[114:115], v56 offset:36936
	s_waitcnt lgkmcnt(3)
	v_mfma_f32_16x16x16_bf16 v[54:57], v[54:55], v[112:113], v[62:65]
	s_nop 2
	v_add_f32_e64 v62, v78, v74
	v_add_f32_e64 v63, v79, v75
	v_pk_add_f32 v[64:65], v[72:73], v[116:117]
	v_pk_add_f32 v[62:63], v[70:71], v[62:63]
	v_add_u32_e32 v74, v144, v107
	s_waitcnt lgkmcnt(2)
	v_mfma_f32_16x16x16_bf16 v[58:61], v[58:59], v[112:113], v[66:69]
	s_nop 2
	v_pk_mov_b32 v[66:67], v[62:63], v[64:65] op_sel:[1,0]
	v_mov_b32_e32 v63, v65
	ds_read_b64_tr_b16 v[64:65], v74 offset:36864
	v_pk_add_f32 v[62:63], v[66:67], v[62:63]
	v_cvt_pk_bf16_f32 v66, v70, v71
	v_add_f32_e32 v75, v62, v63
	v_cvt_pk_bf16_f32 v67, v72, v73
	s_waitcnt lgkmcnt(2)
	v_mfma_f32_16x16x16_bf16 v[42:45], v[76:77], v[112:113], v[42:45]
	ds_read_b64_tr_b16 v[62:63], v74 offset:36872
	ds_read_b64_tr_b16 v[68:69], v74 offset:36928
	ds_read_b64_tr_b16 v[70:71], v74 offset:36936
	s_waitcnt lgkmcnt(3)
	v_mfma_f32_16x16x16_bf16 v[54:57], v[64:65], v[66:67], v[54:57]
	ds_bpermute_b32 v64, v142, v75
	s_waitcnt lgkmcnt(0)
	v_add_f32_e32 v72, v75, v64
	ds_bpermute_b32 v73, v143, v72
	v_mfma_f32_16x16x16_bf16 v[58:61], v[62:63], v[66:67], v[58:61]
	v_mfma_f32_16x16x16_bf16 v[62:65], v[68:69], v[66:67], v[42:45]
	s_waitcnt lgkmcnt(0)
	s_nop 1
	v_add_f32_e32 v43, v72, v73
	v_div_scale_f32 v68, s[64:65], v43, v43, 1.0
	v_mfma_f32_16x16x16_bf16 v[46:49], v[114:115], v[112:113], v[46:49]
	v_rcp_f32_e32 v69, v68
	v_lshlrev_b32_e32 v42, s35, v110
	s_ashr_i32 s35, s34, 31
	v_mfma_f32_16x16x16_bf16 v[44:47], v[70:71], v[66:67], v[46:49]
	s_lshl_b64 s[64:65], s[26:27], 16
	s_lshl_b64 s[34:35], s[34:35], 12
	s_ashr_i32 s26, s31, 31
	s_nop 0
	v_fma_f32 v48, -v68, v69, 1.0
	v_fmac_f32_e32 v69, v48, v69
	v_div_scale_f32 v48, vcc, 1.0, v43, 1.0
	v_mul_f32_e32 v49, v48, v69
	s_add_u32 s31, s34, s31
	v_fma_f32 v66, -v68, v49, v48
	s_addc_u32 s26, s35, s26
	v_fmac_f32_e32 v49, v66, v69
	s_add_u32 s34, s31, s64
	v_fma_f32 v48, -v68, v49, v48
	s_addc_u32 s35, s26, s65
	v_div_fmas_f32 v48, v48, v69, v49
	s_lshl_b32 s26, s30, 7
	s_lshl_b64 s[64:65], s[34:35], 10
	v_div_fixup_f32 v48, v48, v43, 1.0
	s_add_u32 s31, s24, s64
	v_lshl_or_b32 v49, v42, 10, v82
	s_addc_u32 s37, s25, s65
	v_pk_mul_f32 v[54:55], v[48:49], v[54:55] op_sel_hi:[0,1]
	v_pk_mul_f32 v[56:57], v[48:49], v[56:57] op_sel_hi:[0,1]
	s_add_u32 s64, s31, s26
	v_cvt_pk_bf16_f32 v54, v54, v55
	v_cvt_pk_bf16_f32 v55, v56, v57
	v_pk_mul_f32 v[56:57], v[48:49], v[58:59] op_sel_hi:[0,1]
	v_pk_mul_f32 v[58:59], v[48:49], v[60:61] op_sel_hi:[0,1]
	s_addc_u32 s65, s37, 0
	v_cvt_pk_bf16_f32 v56, v56, v57
	v_cvt_pk_bf16_f32 v57, v58, v59
	global_store_dwordx4 v49, v[54:57], s[64:65]
	v_pk_mul_f32 v[44:45], v[48:49], v[44:45] op_sel_hi:[0,1]
	s_nop 0
	v_pk_mul_f32 v[54:55], v[48:49], v[62:63] op_sel_hi:[0,1]
	v_pk_mul_f32 v[56:57], v[48:49], v[64:65] op_sel_hi:[0,1]
	v_cvt_pk_bf16_f32 v54, v54, v55
	v_cvt_pk_bf16_f32 v55, v56, v57
	v_cvt_pk_bf16_f32 v56, v44, v45
	v_pk_mul_f32 v[44:45], v[48:49], v[46:47] op_sel_hi:[0,1]
	v_cvt_pk_bf16_f32 v57, v44, v45
	global_store_dwordx4 v49, v[54:57], s[64:65] offset:64
	s_cmp_eq_u32 s95, 0
	s_cbranch_scc1 .Lcva_skip_l
; __device__ __forceinline__ void titem_finish(const TItem& t, int lane, const LAS unsigned char* buf) {
;     ...
;     if (t.f8) {
; #pragma unroll
;         for (int j = 0; j < 4; ++j) { const int n = (lane >> 3) + 8 * j;
;             int w0 = __builtin_amdgcn_cvt_pk_fp8_f32(v[j][0], v[j][1], 0, false); w0 = __builtin_amdgcn_cvt_pk_fp8_f32(v[j][2], v[j][3], w0, true);
;             int w1 = __builtin_amdgcn_cvt_pk_fp8_f32(v[j][4], v[j][5], 0, false); w1 = __builtin_amdgcn_cvt_pk_fp8_f32(v[j][6], v[j][7], w1, true);
;             u32x2 o; o.x = (unsigned)w0; o.y = (unsigned)w1;
;             __builtin_nontemporal_store(o, (u32x2*)((unsigned char*)t.WT + (size_t)(d0 + n) * t.K + k0 + 8 * c)); }
	s_cmp_eq_u32 s32, 2
	s_cbranch_scc0 .Lcva_skip_l
	s_waitcnt vmcnt(15)
	v_pk_mul_f32 v[168:169], v[168:169], s[94:95] op_sel_hi:[1,0]
	v_pk_mul_f32 v[170:171], v[170:171], s[94:95] op_sel_hi:[1,0]
	v_pk_mul_f32 v[172:173], v[172:173], s[94:95] op_sel_hi:[1,0]
	v_pk_mul_f32 v[174:175], v[174:175], s[94:95] op_sel_hi:[1,0]
	v_pk_mul_f32 v[176:177], v[176:177], s[94:95] op_sel_hi:[1,0]
	v_pk_mul_f32 v[178:179], v[178:179], s[94:95] op_sel_hi:[1,0]
	v_pk_mul_f32 v[180:181], v[180:181], s[94:95] op_sel_hi:[1,0]
	v_pk_mul_f32 v[182:183], v[182:183], s[94:95] op_sel_hi:[1,0]
	v_pk_mul_f32 v[184:185], v[184:185], s[94:95] op_sel_hi:[1,0]
	v_pk_mul_f32 v[186:187], v[186:187], s[94:95] op_sel_hi:[1,0]
	v_pk_mul_f32 v[188:189], v[188:189], s[94:95] op_sel_hi:[1,0]
	v_pk_mul_f32 v[190:191], v[190:191], s[94:95] op_sel_hi:[1,0]
	v_pk_mul_f32 v[192:193], v[192:193], s[94:95] op_sel_hi:[1,0]
	v_pk_mul_f32 v[194:195], v[194:195], s[94:95] op_sel_hi:[1,0]
	v_pk_mul_f32 v[196:197], v[196:197], s[94:95] op_sel_hi:[1,0]
	v_pk_mul_f32 v[198:199], v[198:199], s[94:95] op_sel_hi:[1,0]
	v_pk_mul_f32 v[200:201], v[200:201], s[94:95] op_sel_hi:[1,0]
	v_pk_mul_f32 v[202:203], v[202:203], s[94:95] op_sel_hi:[1,0]
	v_pk_mul_f32 v[204:205], v[204:205], s[94:95] op_sel_hi:[1,0]
	v_pk_mul_f32 v[206:207], v[206:207], s[94:95] op_sel_hi:[1,0]
	v_pk_mul_f32 v[208:209], v[208:209], s[94:95] op_sel_hi:[1,0]
	v_pk_mul_f32 v[210:211], v[210:211], s[94:95] op_sel_hi:[1,0]
	v_pk_mul_f32 v[212:213], v[212:213], s[94:95] op_sel_hi:[1,0]
	v_pk_mul_f32 v[214:215], v[214:215], s[94:95] op_sel_hi:[1,0]
	v_pk_mul_f32 v[216:217], v[216:217], s[94:95] op_sel_hi:[1,0]
	v_pk_mul_f32 v[218:219], v[218:219], s[94:95] op_sel_hi:[1,0]
	v_pk_mul_f32 v[220:221], v[220:221], s[94:95] op_sel_hi:[1,0]
	v_pk_mul_f32 v[222:223], v[222:223], s[94:95] op_sel_hi:[1,0]
	v_pk_mul_f32 v[224:225], v[224:225], s[94:95] op_sel_hi:[1,0]
	v_pk_mul_f32 v[226:227], v[226:227], s[94:95] op_sel_hi:[1,0]
	v_pk_mul_f32 v[228:229], v[228:229], s[94:95] op_sel_hi:[1,0]
	v_pk_mul_f32 v[230:231], v[230:231], s[94:95] op_sel_hi:[1,0]
	s_lshr_b32 s99, s95, 2
	v_lshlrev_b32_e32 v250, 4, v248
	v_cvt_pk_fp8_f32 v232, v168, v172
	v_cvt_pk_fp8_f32 v233, v184, v188
	v_cvt_pk_fp8_f32 v234, v200, v204
	v_cvt_pk_fp8_f32 v235, v216, v220
	v_cvt_pk_fp8_f32 v236, v169, v173
	v_cvt_pk_fp8_f32 v237, v185, v189
	v_cvt_pk_fp8_f32 v238, v201, v205
	v_cvt_pk_fp8_f32 v239, v217, v221
	v_cvt_pk_fp8_f32 v240, v170, v174
	v_cvt_pk_fp8_f32 v241, v186, v190
	v_cvt_pk_fp8_f32 v242, v202, v206
	v_cvt_pk_fp8_f32 v243, v218, v222
	v_cvt_pk_fp8_f32 v244, v171, v175
	v_cvt_pk_fp8_f32 v245, v187, v191
	v_cvt_pk_fp8_f32 v246, v203, v207
	v_cvt_pk_fp8_f32 v247, v219, v223
	v_mad_u32_u24 v250, v249, s99, v250
	v_add_u32_e32 v251, s95, v250
	v_add_u32_e32 v254, s95, v251
	v_add_u32_e32 v255, s95, v254
	v_cvt_pk_fp8_f32 v232, v176, v180 op_sel:[0,0,1]
	v_cvt_pk_fp8_f32 v233, v192, v196 op_sel:[0,0,1]
	v_cvt_pk_fp8_f32 v234, v208, v212 op_sel:[0,0,1]
	v_cvt_pk_fp8_f32 v235, v224, v228 op_sel:[0,0,1]
	v_cvt_pk_fp8_f32 v236, v177, v181 op_sel:[0,0,1]
	v_cvt_pk_fp8_f32 v237, v193, v197 op_sel:[0,0,1]
	v_cvt_pk_fp8_f32 v238, v209, v213 op_sel:[0,0,1]
	v_cvt_pk_fp8_f32 v239, v225, v229 op_sel:[0,0,1]
	v_cvt_pk_fp8_f32 v240, v178, v182 op_sel:[0,0,1]
	v_cvt_pk_fp8_f32 v241, v194, v198 op_sel:[0,0,1]
	v_cvt_pk_fp8_f32 v242, v210, v214 op_sel:[0,0,1]
	v_cvt_pk_fp8_f32 v243, v226, v230 op_sel:[0,0,1]
	v_cvt_pk_fp8_f32 v244, v179, v183 op_sel:[0,0,1]
	v_cvt_pk_fp8_f32 v245, v195, v199 op_sel:[0,0,1]
	v_cvt_pk_fp8_f32 v246, v211, v215 op_sel:[0,0,1]
	v_cvt_pk_fp8_f32 v247, v227, v231 op_sel:[0,0,1]
	global_store_dwordx4 v250, v[232:235], s[92:93] nt
	global_store_dwordx4 v251, v[236:239], s[92:93] nt
	global_store_dwordx4 v254, v[240:243], s[92:93] nt
	global_store_dwordx4 v255, v[244:247], s[92:93] nt

; __device__ __forceinline__ void titem_finish(const TItem& t, int lane, const LAS unsigned char* buf) {
;     ...
;     if (t.f8) {
; #pragma unroll
;         for (int j = 0; j < 4; ++j) { const int n = (lane >> 3) + 8 * j;
;             int w0 = __builtin_amdgcn_cvt_pk_fp8_f32(v[j][0], v[j][1], 0, false); w0 = __builtin_amdgcn_cvt_pk_fp8_f32(v[j][2], v[j][3], w0, true);
;             int w1 = __builtin_amdgcn_cvt_pk_fp8_f32(v[j][4], v[j][5], 0, false); w1 = __builtin_amdgcn_cvt_pk_fp8_f32(v[j][6], v[j][7], w1, true);
;             u32x2 o; o.x = (unsigned)w0; o.y = (unsigned)w1;
;             __builtin_nontemporal_store(o, (u32x2*)((unsigned char*)t.WT + (size_t)(d0 + n) * t.K + k0 + 8 * c)); }
; __device__ __forceinline__ void phase_attn(Frame& F) {
;     ...
;         cu = nu; buf ^= 1;
;     }
;     __syncthreads();
.LBB0_306:
	s_waitcnt vmcnt(0)
	s_cmp_eq_u32 s95, 0
	s_cbranch_scc1 .Lcva_skip_t
	s_cmp_eq_u32 s32, 3
	s_cbranch_scc0 .Lcva_skip_t
	s_waitcnt vmcnt(0)
	v_pk_mul_f32 v[168:169], v[168:169], s[94:95] op_sel_hi:[1,0]
	v_pk_mul_f32 v[170:171], v[170:171], s[94:95] op_sel_hi:[1,0]
	v_pk_mul_f32 v[172:173], v[172:173], s[94:95] op_sel_hi:[1,0]
	v_pk_mul_f32 v[174:175], v[174:175], s[94:95] op_sel_hi:[1,0]
	v_pk_mul_f32 v[176:177], v[176:177], s[94:95] op_sel_hi:[1,0]
	v_pk_mul_f32 v[178:179], v[178:179], s[94:95] op_sel_hi:[1,0]
	v_pk_mul_f32 v[180:181], v[180:181], s[94:95] op_sel_hi:[1,0]
	v_pk_mul_f32 v[182:183], v[182:183], s[94:95] op_sel_hi:[1,0]
	v_pk_mul_f32 v[184:185], v[184:185], s[94:95] op_sel_hi:[1,0]
	v_pk_mul_f32 v[186:187], v[186:187], s[94:95] op_sel_hi:[1,0]
	v_pk_mul_f32 v[188:189], v[188:189], s[94:95] op_sel_hi:[1,0]
	v_pk_mul_f32 v[190:191], v[190:191], s[94:95] op_sel_hi:[1,0]
	v_pk_mul_f32 v[192:193], v[192:193], s[94:95] op_sel_hi:[1,0]
	v_pk_mul_f32 v[194:195], v[194:195], s[94:95] op_sel_hi:[1,0]
	v_pk_mul_f32 v[196:197], v[196:197], s[94:95] op_sel_hi:[1,0]
	v_pk_mul_f32 v[198:199], v[198:199], s[94:95] op_sel_hi:[1,0]
	v_pk_mul_f32 v[200:201], v[200:201], s[94:95] op_sel_hi:[1,0]
	v_pk_mul_f32 v[202:203], v[202:203], s[94:95] op_sel_hi:[1,0]
	v_pk_mul_f32 v[204:205], v[204:205], s[94:95] op_sel_hi:[1,0]
	v_pk_mul_f32 v[206:207], v[206:207], s[94:95] op_sel_hi:[1,0]
	v_pk_mul_f32 v[208:209], v[208:209], s[94:95] op_sel_hi:[1,0]
	v_pk_mul_f32 v[210:211], v[210:211], s[94:95] op_sel_hi:[1,0]
	v_pk_mul_f32 v[212:213], v[212:213], s[94:95] op_sel_hi:[1,0]
	v_pk_mul_f32 v[214:215], v[214:215], s[94:95] op_sel_hi:[1,0]
	v_pk_mul_f32 v[216:217], v[216:217], s[94:95] op_sel_hi:[1,0]
	v_pk_mul_f32 v[218:219], v[218:219], s[94:95] op_sel_hi:[1,0]
	v_pk_mul_f32 v[220:221], v[220:221], s[94:95] op_sel_hi:[1,0]
	v_pk_mul_f32 v[222:223], v[222:223], s[94:95] op_sel_hi:[1,0]
	v_pk_mul_f32 v[224:225], v[224:225], s[94:95] op_sel_hi:[1,0]
	v_pk_mul_f32 v[226:227], v[226:227], s[94:95] op_sel_hi:[1,0]
	v_pk_mul_f32 v[228:229], v[228:229], s[94:95] op_sel_hi:[1,0]
	v_pk_mul_f32 v[230:231], v[230:231], s[94:95] op_sel_hi:[1,0]
	s_lshr_b32 s99, s95, 2
	v_lshlrev_b32_e32 v250, 4, v248
	v_cvt_pk_fp8_f32 v232, v168, v172
	v_cvt_pk_fp8_f32 v233, v184, v188
	v_cvt_pk_fp8_f32 v234, v200, v204
	v_cvt_pk_fp8_f32 v235, v216, v220
	v_cvt_pk_fp8_f32 v236, v169, v173
	v_cvt_pk_fp8_f32 v237, v185, v189
	v_cvt_pk_fp8_f32 v238, v201, v205
	v_cvt_pk_fp8_f32 v239, v217, v221
	v_cvt_pk_fp8_f32 v240, v170, v174
	v_cvt_pk_fp8_f32 v241, v186, v190
	v_cvt_pk_fp8_f32 v242, v202, v206
	v_cvt_pk_fp8_f32 v243, v218, v222
	v_cvt_pk_fp8_f32 v244, v171, v175
	v_cvt_pk_fp8_f32 v245, v187, v191
	v_cvt_pk_fp8_f32 v246, v203, v207
	v_cvt_pk_fp8_f32 v247, v219, v223
	v_mad_u32_u24 v250, v249, s99, v250
	v_add_u32_e32 v251, s95, v250
	v_add_u32_e32 v254, s95, v251
	v_add_u32_e32 v255, s95, v254
	v_cvt_pk_fp8_f32 v232, v176, v180 op_sel:[0,0,1]
	v_cvt_pk_fp8_f32 v233, v192, v196 op_sel:[0,0,1]
	v_cvt_pk_fp8_f32 v234, v208, v212 op_sel:[0,0,1]
	v_cvt_pk_fp8_f32 v235, v224, v228 op_sel:[0,0,1]
	v_cvt_pk_fp8_f32 v236, v177, v181 op_sel:[0,0,1]
	v_cvt_pk_fp8_f32 v237, v193, v197 op_sel:[0,0,1]
	v_cvt_pk_fp8_f32 v238, v209, v213 op_sel:[0,0,1]
	v_cvt_pk_fp8_f32 v239, v225, v229 op_sel:[0,0,1]
	v_cvt_pk_fp8_f32 v240, v178, v182 op_sel:[0,0,1]
	v_cvt_pk_fp8_f32 v241, v194, v198 op_sel:[0,0,1]
	v_cvt_pk_fp8_f32 v242, v210, v214 op_sel:[0,0,1]
	v_cvt_pk_fp8_f32 v243, v226, v230 op_sel:[0,0,1]
	v_cvt_pk_fp8_f32 v244, v179, v183 op_sel:[0,0,1]
	v_cvt_pk_fp8_f32 v245, v195, v199 op_sel:[0,0,1]
	v_cvt_pk_fp8_f32 v246, v211, v215 op_sel:[0,0,1]
	v_cvt_pk_fp8_f32 v247, v227, v231 op_sel:[0,0,1]
	global_store_dwordx4 v250, v[232:235], s[92:93] nt
	global_store_dwordx4 v251, v[236:239], s[92:93] nt
	global_store_dwordx4 v254, v[240:243], s[92:93] nt
	global_store_dwordx4 v255, v[244:247], s[92:93] nt
